# attention phases: static s_setprio 1 for waves 4-7
# baseline (speedup 1.0000x reference)
.LBB0_472:
	s_cmp_ge_u32 s91, 4
	s_cbranch_scc0 .Lprio3_skip
	s_setprio 1

.LBB0_566:
	s_setprio 0
	s_cmp_lt_i32 s57, 5
	s_cbranch_scc1 .LBB0_616
	s_waitcnt vmcnt(0)
	v_cmp_eq_u32_e32 vcc, 0, v0
	s_waitcnt lgkmcnt(0)
	s_barrier
	s_and_saveexec_b64 s[0:1], vcc
	s_cbranch_execz .LBB0_615
	v_readlane_b32 s2, v255, 22
	s_waitcnt vmcnt(0) expcnt(0) lgkmcnt(0)
	s_nop 0
	v_mov_b32_e32 v1, s2
	ds_read_b32 v3, v1
	ds_read_b32 v1, v1 offset:4
	s_waitcnt lgkmcnt(1)
	v_cmp_ne_u32_e32 vcc, 0, v3
	s_cbranch_vccnz .LBB0_583
	v_readlane_b32 s2, v255, 1
	v_readlane_b32 s3, v255, 2
	s_load_dwordx2 s[6:7], s[2:3], 0x4
	s_add_u32 s2, s92, 0x4200
	s_addc_u32 s3, s93, 0
	s_add_u32 s4, s92, 0x4400
	s_addc_u32 s5, s93, 0
	s_waitcnt lgkmcnt(0)
	s_mul_i32 s33, s6, s84
	s_add_u32 s6, s92, 0x4500
	s_mul_i32 s33, s33, s7
	s_addc_u32 s7, s93, 0
	s_add_u32 s8, s92, 0x4600
	s_addc_u32 s9, s93, 0
	s_add_u32 s10, s92, 0x4700
	s_addc_u32 s11, s93, 0
	s_add_u32 s12, s92, 0x4800
	s_addc_u32 s13, s93, 0
	s_add_u32 s14, s92, 0x4900
	s_addc_u32 s15, s93, 0
	s_add_u32 s16, s92, 0x4a00
	s_addc_u32 s17, s93, 0
	s_add_u32 s18, s92, 0x4b00
	s_addc_u32 s19, s93, 0
	s_add_u32 s20, s92, 0x4c00
	s_addc_u32 s21, s93, 0
	s_add_u32 s22, s92, 0x4d00
	s_addc_u32 s23, s93, 0
	s_add_u32 s24, s92, 0x4e00
	s_addc_u32 s25, s93, 0
	s_add_u32 s26, s92, 0x4f00
	s_addc_u32 s27, s93, 0
	s_add_u32 s28, s92, 0x5000
	s_addc_u32 s29, s93, 0
	s_add_u32 s30, s92, 0x5100
	s_addc_u32 s31, s93, 0
	s_add_u32 s34, s92, 0x5200
	s_addc_u32 s35, s93, 0
	s_add_u32 s38, s92, 0x5300
	s_addc_u32 s39, s93, 0
	s_mov_b32 s47, 1
	v_mov_b32_e32 v17, 0
	s_branch .LBB0_571

.LBB0_699:
	s_setprio 0
	s_cmp_lt_i32 s57, 6
	s_barrier
	s_cbranch_scc1 .LBB0_749
	s_waitcnt vmcnt(0)
	v_cmp_eq_u32_e32 vcc, 0, v0
	s_barrier
	s_and_saveexec_b64 s[0:1], vcc
	s_cbranch_execz .LBB0_748
	v_readlane_b32 s2, v255, 22
	s_waitcnt vmcnt(0) expcnt(0) lgkmcnt(0)
	s_nop 0
	v_mov_b32_e32 v1, s2
	ds_read_b32 v3, v1
	ds_read_b32 v1, v1 offset:4
	s_waitcnt lgkmcnt(1)
	v_cmp_ne_u32_e32 vcc, 0, v3
	s_cbranch_vccnz .LBB0_716
	v_readlane_b32 s2, v255, 1
	v_readlane_b32 s3, v255, 2
	s_load_dwordx2 s[6:7], s[2:3], 0x4
	s_add_u32 s2, s92, 0x4200
	s_addc_u32 s3, s93, 0
	s_add_u32 s4, s92, 0x4400
	s_addc_u32 s5, s93, 0
	s_waitcnt lgkmcnt(0)
	s_mul_i32 s33, s6, s84
	s_add_u32 s6, s92, 0x4500
	s_mul_i32 s33, s33, s7
	s_addc_u32 s7, s93, 0
	s_add_u32 s8, s92, 0x4600
	s_addc_u32 s9, s93, 0
	s_add_u32 s10, s92, 0x4700
	s_addc_u32 s11, s93, 0
	s_add_u32 s12, s92, 0x4800
	s_addc_u32 s13, s93, 0
	s_add_u32 s14, s92, 0x4900
	s_addc_u32 s15, s93, 0
	s_add_u32 s16, s92, 0x4a00
	s_addc_u32 s17, s93, 0
	s_add_u32 s18, s92, 0x4b00
	s_addc_u32 s19, s93, 0
	s_add_u32 s20, s92, 0x4c00
	s_addc_u32 s21, s93, 0
	s_add_u32 s22, s92, 0x4d00
	s_addc_u32 s23, s93, 0
	s_add_u32 s24, s92, 0x4e00
	s_addc_u32 s25, s93, 0
	s_add_u32 s26, s92, 0x4f00
	s_addc_u32 s27, s93, 0
	s_add_u32 s28, s92, 0x5000
	s_addc_u32 s29, s93, 0
	s_add_u32 s30, s92, 0x5100
	s_addc_u32 s31, s93, 0
	s_add_u32 s34, s92, 0x5200
	s_addc_u32 s35, s93, 0
	s_add_u32 s38, s92, 0x5300
	s_addc_u32 s39, s93, 0
	s_mov_b32 s46, 1
	v_mov_b32_e32 v17, 0
	s_branch .LBB0_704
